# custom fp8 conversion helper (73 helper WGs) + router unpack moved + P11 g_fin loads hoisted out of the token loop
# speedup vs baseline: 1.0091x; 1.0091x over previous
; #define GAS __attribute__((address_space(1)))
; __device__ __forceinline__ void p11_combine(const P& p, int gw, int NGW, int lane, float oscale) {
;     const int* cnt = (const int*)(p.ws + WS_CTL) + CW_CNT; const unsigned char* Y = (const unsigned char*)(p.ws + WS_Y);
;     const int* tope = (const int*)(p.ws + WS_TOPE); const float* topg = (const float*)(p.ws + WS_TOPG); const int* tpos = (const int*)(p.ws + WS_TPOS);
;     int pad = lane < NE ? ((cnt[lane & 31] + 255) >> 8) : 0; int inc = pad;
; #pragma unroll
;     for (int o = 1; o < 32; o <<= 1) { const int t = __shfl_up(inc, o); if ((lane & 31) >= o) inc += t; }
;     const int toff_l = inc - pad;
;     for (int m = gw; m < NTOK; m += NGW) {
;         GAS f32x4* xr = (GAS f32x4*)(p.out + (size_t)m * DM) + lane;
;         const GAS v2u* x2r = (const GAS v2u*)((const bf16*)(p.ws + WS_X2H) + (size_t)m * DM) + lane;
;     ...
;         const GAS f32x4* gf = (const GAS f32x4*)p.g_fin + lane;
; #pragma unroll
;         for (int j = 0; j < 8; ++j) { const f32x4 g = gf[64 * j]; xr[64 * j] = a[j] * r * g; }
.LBB5_1740:
	s_or_b64 exec, exec, s[0:1]
	v_mbcnt_lo_u32_b32 v1, -1, 0
	v_mbcnt_hi_u32_b32 v1, -1, v1
	v_and_b32_e32 v38, 64, v1
	v_add_u32_e32 v3, -1, v1
	v_cmp_lt_i32_e32 vcc, v3, v38
	v_and_b32_e32 v0, 31, v0
	s_waitcnt lgkmcnt(0)
	v_add_u32_e32 v4, -2, v1
	v_cndmask_b32_e32 v3, v3, v1, vcc
	v_lshlrev_b32_e32 v3, 2, v3
	ds_bpermute_b32 v3, v3, v2
	v_cmp_ne_u32_e32 vcc, 0, v0
	s_cmpk_gt_i32 s28, 0x7fff
	s_waitcnt lgkmcnt(0)
	v_cndmask_b32_e32 v3, 0, v3, vcc
	v_cmp_lt_i32_e32 vcc, v4, v38
	v_add_u32_e32 v3, v3, v2
	s_nop 0
	v_cndmask_b32_e32 v4, v4, v1, vcc
	v_lshlrev_b32_e32 v4, 2, v4
	ds_bpermute_b32 v4, v4, v3
	v_cmp_lt_u32_e32 vcc, 1, v0
	s_waitcnt lgkmcnt(0)
	s_nop 0
	v_cndmask_b32_e32 v4, 0, v4, vcc
	v_add_u32_e32 v3, v4, v3
	v_add_u32_e32 v4, -4, v1
	v_cmp_lt_i32_e32 vcc, v4, v38
	s_nop 1
	v_cndmask_b32_e32 v4, v4, v1, vcc
	v_lshlrev_b32_e32 v4, 2, v4
	ds_bpermute_b32 v4, v4, v3
	v_cmp_lt_u32_e32 vcc, 3, v0
	s_waitcnt lgkmcnt(0)
	s_nop 0
	v_cndmask_b32_e32 v4, 0, v4, vcc
	v_add_u32_e32 v3, v4, v3
	v_add_u32_e32 v4, -8, v1
	v_cmp_lt_i32_e32 vcc, v4, v38
	s_nop 1
	v_cndmask_b32_e32 v4, v4, v1, vcc
	v_lshlrev_b32_e32 v4, 2, v4
	ds_bpermute_b32 v4, v4, v3
	v_cmp_lt_u32_e32 vcc, 7, v0
	s_waitcnt lgkmcnt(0)
	s_nop 0
	v_cndmask_b32_e32 v4, 0, v4, vcc
	v_add_u32_e32 v3, v4, v3
	v_add_u32_e32 v4, -16, v1
	v_cmp_lt_i32_e32 vcc, v4, v38
	s_nop 1
	v_cndmask_b32_e32 v4, v4, v1, vcc
	v_lshlrev_b32_e32 v4, 2, v4
	ds_bpermute_b32 v4, v4, v3
	s_cbranch_scc1 .LBB5_1743
	v_cmp_lt_u32_e32 vcc, 15, v0
	v_sub_u32_e32 v2, v3, v2
	v_readlane_b32 s12, v253, 2
	s_waitcnt lgkmcnt(0)
	v_cndmask_b32_e32 v0, 0, v4, vcc
	v_add_u32_e32 v39, v2, v0
	v_add_u32_e32 v0, 64, v38
	v_xor_b32_e32 v2, 1, v1
	v_cmp_lt_i32_e32 vcc, v2, v0
	s_add_u32 s6, s22, 0x3100000
	v_lshlrev_b32_e32 v4, 4, v198
	v_cndmask_b32_e32 v2, v1, v2, vcc
	v_lshlrev_b32_e32 v40, 2, v2
	v_xor_b32_e32 v2, 2, v1
	v_cmp_lt_i32_e32 vcc, v2, v0
	v_mov_b32_e32 v5, 0
	v_readlane_b32 s18, v253, 8
	v_cndmask_b32_e32 v2, v1, v2, vcc
	v_lshlrev_b32_e32 v41, 2, v2
	v_xor_b32_e32 v2, 4, v1
	v_cmp_lt_i32_e32 vcc, v2, v0
	v_readlane_b32 s19, v253, 9
	s_addc_u32 s7, s23, 0
	v_cndmask_b32_e32 v2, v1, v2, vcc
	v_lshlrev_b32_e32 v42, 2, v2
	v_xor_b32_e32 v2, 8, v1
	v_cmp_lt_i32_e32 vcc, v2, v0
	v_lshl_add_u64 v[6:7], s[18:19], 0, v[4:5]
	s_mov_b64 s[0:1], 0x1400
	v_cndmask_b32_e32 v2, v1, v2, vcc
	v_lshlrev_b32_e32 v43, 2, v2
	v_xor_b32_e32 v2, 16, v1
	v_cmp_lt_i32_e32 vcc, v2, v0
	s_add_u32 s8, s22, 0x3180000
	v_lshl_add_u64 v[10:11], v[6:7], 0, s[0:1]
	v_cndmask_b32_e32 v2, v1, v2, vcc
	v_lshlrev_b32_e32 v44, 2, v2
	v_xor_b32_e32 v2, 32, v1
	v_cmp_lt_i32_e32 vcc, v2, v0
	s_mov_b64 s[0:1], 0x1800
	s_addc_u32 s9, s23, 0
	v_cndmask_b32_e32 v0, v1, v2, vcc
	v_lshlrev_b32_e32 v45, 2, v0
	v_lshl_add_u64 v[12:13], v[6:7], 0, s[0:1]
	s_mov_b64 s[0:1], 0x1c00
	v_lshlrev_b32_e32 v0, 2, v198
	v_mov_b32_e32 v1, v5
	s_add_u32 s10, s22, 0x3200000
	v_lshl_add_u64 v[14:15], v[6:7], 0, s[0:1]
	v_lshl_add_u64 v[0:1], s[22:23], 0, v[0:1]
	s_mov_b64 s[0:1], 0x8a000000
	s_addc_u32 s11, s23, 0
	v_lshl_add_u64 v[16:17], v[0:1], 0, s[0:1]
	s_lshl_b32 s0, s94, 5
	s_lshl_b32 s1, s95, 2
	s_ashr_i32 s29, s28, 31
	s_add_i32 s0, s0, s1
	s_lshl_b32 s12, s33, 5
	s_lshl_b64 s[4:5], s[28:29], 13
	s_add_u32 s4, s20, s4
	s_addc_u32 s5, s21, s5
	s_mov_b64 s[2:3], 0x1000
	v_lshl_add_u64 v[0:1], s[4:5], 0, v[4:5]
	s_ashr_i32 s27, s26, 31
	v_lshl_add_u64 v[8:9], v[6:7], 0, s[2:3]
	v_lshl_add_u64 v[18:19], v[0:1], 0, s[2:3]
	s_lshl_b64 s[2:3], s[26:27], 13
	s_lshl_b64 s[4:5], s[28:29], 12
	s_add_u32 s4, s22, s4
	v_lshlrev_b32_e32 v4, 3, v198
	s_addc_u32 s5, s23, s5
	v_readlane_b32 s13, v253, 3
	v_lshl_add_u64 v[0:1], s[4:5], 0, v[4:5]
	s_mov_b64 s[4:5], 0xac000000
	v_lshl_add_u64 v[20:21], v[0:1], 0, s[4:5]
	s_lshl_b64 s[4:5], s[26:27], 12
	v_mov_b32_e32 v4, 0x358637bd
	s_mov_b32 s13, 0x800000
	v_readlane_b32 s14, v253, 4
	v_readlane_b32 s15, v253, 5
	v_readlane_b32 s16, v253, 6
	v_readlane_b32 s17, v253, 7
	global_load_dwordx4 v[164:167], v[6:7], off offset:1024
	global_load_dwordx4 v[168:171], v[6:7], off offset:2048
	global_load_dwordx4 v[172:175], v[6:7], off offset:3072
	global_load_dwordx4 v[176:179], v[8:9], off
	global_load_dwordx4 v[180:183], v[10:11], off
	global_load_dwordx4 v[184:187], v[12:13], off
	global_load_dwordx4 v[188:191], v[14:15], off
; #define GAS __attribute__((address_space(1)))
; __device__ __forceinline__ void p11_combine(const P& p, int gw, int NGW, int lane, float oscale) {
;     ...
;     for (int m = gw; m < NTOK; m += NGW) {
;         GAS f32x4* xr = (GAS f32x4*)(p.out + (size_t)m * DM) + lane;
;         const GAS v2u* x2r = (const GAS v2u*)((const bf16*)(p.ws + WS_X2H) + (size_t)m * DM) + lane;
;         f32x4 a[8];
; #pragma unroll
;         for (int j = 0; j < 8; ++j) { const v2u w = x2r[64 * j]; a[j] = (f32x4){__uint_as_float(w.x << 16), __uint_as_float(w.x & 0xffff0000u), __uint_as_float(w.y << 16), __uint_as_float(w.y & 0xffff0000u)}; }
; #pragma unroll
;         for (int k = 0; k < TOPK; ++k) { const int e = tope[m * 4 + k]; const float g = topg[m * 4 + k]; const int slot = 256 * __shfl(toff_l, e) + tpos[m * 4 + k];
;             const GAS unsigned* yr = (const GAS unsigned*)(Y + (size_t)slot * DM) + lane;
; #pragma unroll
;             for (int j = 0; j < 8; ++j) { const int w = (int)yr[64 * j]; const f32x2 lo = __builtin_amdgcn_cvt_pk_f32_fp8(w, false), hi = __builtin_amdgcn_cvt_pk_f32_fp8(w, true);
;                 a[j].x += g * lo.x; a[j].y += g * lo.y; a[j].z += g * hi.x; a[j].w += g * hi.y; } }
.LBB5_1742:
	s_ashr_i32 s1, s0, 31
	s_lshl_b64 s[14:15], s[0:1], 2
	s_add_u32 s16, s6, s14
	s_addc_u32 s17, s7, s15
	global_load_dwordx2 v[36:37], v[20:21], off
	global_load_dwordx2 v[34:35], v[20:21], off offset:512
	global_load_dwordx2 v[32:33], v[20:21], off offset:1024
	global_load_dwordx2 v[30:31], v[20:21], off offset:1536
	global_load_dwordx2 v[28:29], v[20:21], off offset:2048
	global_load_dwordx2 v[26:27], v[20:21], off offset:2560
	global_load_dwordx2 v[24:25], v[20:21], off offset:3072
	global_load_dwordx2 v[22:23], v[20:21], off offset:3584
	global_load_dwordx4 v[46:49], v5, s[16:17]
	s_add_u32 s16, s8, s14
	s_addc_u32 s17, s9, s15
	s_add_u32 s14, s10, s14
	s_addc_u32 s15, s11, s15
	global_load_dword v54, v5, s[16:17]
	global_load_dword v53, v5, s[14:15]
	s_add_i32 s16, s0, 1
	s_ashr_i32 s17, s16, 31
	s_lshl_b64 s[14:15], s[16:17], 2
	s_add_u32 s16, s8, s14
	s_addc_u32 s17, s9, s15
	s_add_u32 s14, s10, s14
	s_addc_u32 s15, s11, s15
	global_load_dwordx3 v[50:52], v5, s[16:17]
	global_load_dword v55, v5, s[14:15]
	s_add_i32 s16, s0, 2
	s_ashr_i32 s17, s16, 31
	s_lshl_b64 s[14:15], s[16:17], 2
	s_add_u32 s14, s10, s14
	s_addc_u32 s15, s11, s15
	global_load_dwordx2 v[56:57], v5, s[14:15]
	global_load_dwordx4 v[0:3], v[6:7], off
	s_add_i32 s28, s28, s26
	s_add_i32 s0, s0, s12
	v_lshl_add_u64 v[20:21], v[20:21], 0, s[4:5]
	s_cmp_lt_i32 s28, 0x8000
	s_waitcnt vmcnt(14)
	v_lshlrev_b32_e32 v58, 16, v36
	v_and_b32_e32 v59, 0xffff0000, v36
	v_lshlrev_b32_e32 v36, 16, v37
	v_and_b32_e32 v37, 0xffff0000, v37
	s_waitcnt vmcnt(13)
	v_lshlrev_b32_e32 v60, 16, v34
	v_and_b32_e32 v61, 0xffff0000, v34
	v_lshlrev_b32_e32 v34, 16, v35
	v_and_b32_e32 v35, 0xffff0000, v35
	s_waitcnt vmcnt(6)
	v_and_or_b32 v46, v46, 63, v38
	v_lshlrev_b32_e32 v46, 2, v46
	v_and_or_b32 v47, v47, 63, v38
	ds_bpermute_b32 v46, v46, v39
	v_lshlrev_b32_e32 v47, 2, v47
	ds_bpermute_b32 v74, v47, v39
	v_and_or_b32 v48, v48, 63, v38
	v_and_or_b32 v49, v49, 63, v38
	v_lshlrev_b32_e32 v48, 2, v48
	s_waitcnt vmcnt(4) lgkmcnt(1)
	v_lshl_add_u32 v46, v46, 8, v53
	v_lshlrev_b32_e32 v49, 2, v49
	ds_bpermute_b32 v75, v48, v39
	v_ashrrev_i32_e32 v47, 31, v46
	ds_bpermute_b32 v49, v49, v39
	s_waitcnt vmcnt(3)
	v_mov_b32_e32 v48, v52
	v_lshlrev_b64 v[46:47], 11, v[46:47]
	s_waitcnt vmcnt(2) lgkmcnt(2)
	v_lshl_add_u32 v52, v74, 8, v55
	v_lshl_add_u64 v[46:47], v[16:17], 0, v[46:47]
	v_ashrrev_i32_e32 v53, 31, v52
	global_load_dword v55, v[46:47], off
	global_load_dword v74, v[46:47], off offset:256
	global_load_dword v78, v[46:47], off offset:512
	global_load_dword v82, v[46:47], off offset:768
	global_load_dword v86, v[46:47], off offset:1024
	global_load_dword v90, v[46:47], off offset:1280
	global_load_dword v94, v[46:47], off offset:1536
	global_load_dword v98, v[46:47], off offset:1792
	v_lshlrev_b64 v[46:47], 11, v[52:53]
	v_lshl_add_u64 v[46:47], v[16:17], 0, v[46:47]
	global_load_dword v102, v[46:47], off
	global_load_dword v106, v[46:47], off offset:256
	global_load_dword v110, v[46:47], off offset:512
	global_load_dword v114, v[46:47], off offset:768
	global_load_dword v118, v[46:47], off offset:1024
	global_load_dword v122, v[46:47], off offset:1280
	global_load_dword v126, v[46:47], off offset:1536
	global_load_dword v130, v[46:47], off offset:1792
	s_waitcnt vmcnt(17) lgkmcnt(1)
	v_lshl_add_u32 v46, v75, 8, v56
	s_waitcnt lgkmcnt(0)
	v_lshl_add_u32 v52, v49, 8, v57
	v_ashrrev_i32_e32 v47, 31, v46
	v_ashrrev_i32_e32 v53, 31, v52
	v_lshlrev_b64 v[46:47], 11, v[46:47]
	v_lshlrev_b64 v[52:53], 11, v[52:53]
	v_lshl_add_u64 v[46:47], v[16:17], 0, v[46:47]
	v_lshl_add_u64 v[52:53], v[16:17], 0, v[52:53]
	global_load_dword v49, v[46:47], off
	global_load_dword v132, v[46:47], off offset:256
	global_load_dword v133, v[46:47], off offset:512
	global_load_dword v134, v[46:47], off offset:768
	global_load_dword v135, v[46:47], off offset:1024
	global_load_dword v136, v[46:47], off offset:1280
	global_load_dword v137, v[46:47], off offset:1536
	global_load_dword v138, v[46:47], off offset:1792
	global_load_dword v139, v[52:53], off
	global_load_dword v140, v[52:53], off offset:256
	global_load_dword v141, v[52:53], off offset:512
	global_load_dword v142, v[52:53], off offset:768
	global_load_dword v143, v[52:53], off offset:1024
	global_load_dword v144, v[52:53], off offset:1280
	global_load_dword v145, v[52:53], off offset:1536
	global_load_dword v146, v[52:53], off offset:1792
	v_lshlrev_b32_e32 v62, 16, v32
	v_and_b32_e32 v63, 0xffff0000, v32
	v_lshlrev_b32_e32 v32, 16, v33
	v_and_b32_e32 v33, 0xffff0000, v33
	v_lshlrev_b32_e32 v64, 16, v30
	v_and_b32_e32 v65, 0xffff0000, v30
	v_lshlrev_b32_e32 v30, 16, v31
	v_and_b32_e32 v31, 0xffff0000, v31
	v_lshlrev_b32_e32 v66, 16, v28
	v_and_b32_e32 v67, 0xffff0000, v28
	v_lshlrev_b32_e32 v28, 16, v29
	v_and_b32_e32 v29, 0xffff0000, v29
	v_lshlrev_b32_e32 v68, 16, v26
	v_and_b32_e32 v69, 0xffff0000, v26
	v_lshlrev_b32_e32 v26, 16, v27
	v_and_b32_e32 v27, 0xffff0000, v27
	v_lshlrev_b32_e32 v70, 16, v24
	v_and_b32_e32 v71, 0xffff0000, v24
	v_lshlrev_b32_e32 v24, 16, v25
	v_and_b32_e32 v25, 0xffff0000, v25
	v_lshlrev_b32_e32 v72, 16, v22
	v_and_b32_e32 v73, 0xffff0000, v22
	v_lshlrev_b32_e32 v22, 16, v23
	v_and_b32_e32 v23, 0xffff0000, v23
	s_waitcnt vmcnt(31)
	v_cvt_pk_f32_fp8_e32 v[46:47], v55
	v_cvt_pk_f32_fp8_sdwa v[52:53], v55 src0_sel:WORD_1
	s_waitcnt vmcnt(30)
	v_cvt_pk_f32_fp8_e32 v[56:57], v74
	v_cvt_pk_f32_fp8_sdwa v[74:75], v74 src0_sel:WORD_1
	s_waitcnt vmcnt(29)
	v_cvt_pk_f32_fp8_e32 v[76:77], v78
	v_cvt_pk_f32_fp8_sdwa v[78:79], v78 src0_sel:WORD_1
	s_waitcnt vmcnt(28)
	v_cvt_pk_f32_fp8_e32 v[80:81], v82
	v_cvt_pk_f32_fp8_sdwa v[82:83], v82 src0_sel:WORD_1
	s_waitcnt vmcnt(27)
; #define GAS __attribute__((address_space(1)))
; __device__ __forceinline__ void p11_combine(const P& p, int gw, int NGW, int lane, float oscale) {
;     ...
;         for (int k = 0; k < TOPK; ++k) { const int e = tope[m * 4 + k]; const float g = topg[m * 4 + k]; const int slot = 256 * __shfl(toff_l, e) + tpos[m * 4 + k];
;             const GAS unsigned* yr = (const GAS unsigned*)(Y + (size_t)slot * DM) + lane;
; #pragma unroll
;             for (int j = 0; j < 8; ++j) { const int w = (int)yr[64 * j]; const f32x2 lo = __builtin_amdgcn_cvt_pk_f32_fp8(w, false), hi = __builtin_amdgcn_cvt_pk_f32_fp8(w, true);
;                 a[j].x += g * lo.x; a[j].y += g * lo.y; a[j].z += g * hi.x; a[j].w += g * hi.y; } }
	v_cvt_pk_f32_fp8_e32 v[84:85], v86
	v_cvt_pk_f32_fp8_sdwa v[86:87], v86 src0_sel:WORD_1
	s_waitcnt vmcnt(26)
	v_cvt_pk_f32_fp8_e32 v[88:89], v90
	v_cvt_pk_f32_fp8_sdwa v[90:91], v90 src0_sel:WORD_1
	s_waitcnt vmcnt(25)
	v_cvt_pk_f32_fp8_e32 v[92:93], v94
	v_cvt_pk_f32_fp8_sdwa v[94:95], v94 src0_sel:WORD_1
	s_waitcnt vmcnt(24)
	v_cvt_pk_f32_fp8_e32 v[96:97], v98
	v_cvt_pk_f32_fp8_sdwa v[98:99], v98 src0_sel:WORD_1
	s_waitcnt vmcnt(23)
	v_cvt_pk_f32_fp8_e32 v[100:101], v102
	v_cvt_pk_f32_fp8_sdwa v[102:103], v102 src0_sel:WORD_1
	s_waitcnt vmcnt(22)
	v_cvt_pk_f32_fp8_e32 v[104:105], v106
	v_cvt_pk_f32_fp8_sdwa v[106:107], v106 src0_sel:WORD_1
	s_waitcnt vmcnt(21)
	v_cvt_pk_f32_fp8_e32 v[108:109], v110
	s_waitcnt vmcnt(20)
	v_cvt_pk_f32_fp8_e32 v[112:113], v114
	s_waitcnt vmcnt(19)
	v_cvt_pk_f32_fp8_e32 v[116:117], v118
	s_waitcnt vmcnt(18)
	v_cvt_pk_f32_fp8_e32 v[120:121], v122
	s_waitcnt vmcnt(17)
	v_cvt_pk_f32_fp8_e32 v[124:125], v126
	v_cvt_pk_f32_fp8_sdwa v[110:111], v110 src0_sel:WORD_1
	v_cvt_pk_f32_fp8_sdwa v[114:115], v114 src0_sel:WORD_1
	v_cvt_pk_f32_fp8_sdwa v[118:119], v118 src0_sel:WORD_1
	v_cvt_pk_f32_fp8_sdwa v[122:123], v122 src0_sel:WORD_1
	v_cvt_pk_f32_fp8_sdwa v[126:127], v126 src0_sel:WORD_1
	s_waitcnt vmcnt(16)
	v_cvt_pk_f32_fp8_e32 v[128:129], v130
	v_cvt_pk_f32_fp8_sdwa v[130:131], v130 src0_sel:WORD_1
	v_pk_fma_f32 v[46:47], v[54:55], v[46:47], v[58:59] op_sel_hi:[0,1,1]
	v_pk_fma_f32 v[36:37], v[54:55], v[52:53], v[36:37] op_sel_hi:[0,1,1]
	v_pk_fma_f32 v[52:53], v[54:55], v[56:57], v[60:61] op_sel_hi:[0,1,1]
	v_pk_fma_f32 v[34:35], v[54:55], v[74:75], v[34:35] op_sel_hi:[0,1,1]
	v_pk_fma_f32 v[56:57], v[54:55], v[76:77], v[62:63] op_sel_hi:[0,1,1]
	v_pk_fma_f32 v[32:33], v[54:55], v[78:79], v[32:33] op_sel_hi:[0,1,1]
	v_pk_fma_f32 v[58:59], v[54:55], v[80:81], v[64:65] op_sel_hi:[0,1,1]
	v_pk_fma_f32 v[30:31], v[54:55], v[82:83], v[30:31] op_sel_hi:[0,1,1]
	v_pk_fma_f32 v[60:61], v[54:55], v[84:85], v[66:67] op_sel_hi:[0,1,1]
	v_pk_fma_f32 v[28:29], v[54:55], v[86:87], v[28:29] op_sel_hi:[0,1,1]
	v_pk_fma_f32 v[62:63], v[54:55], v[88:89], v[68:69] op_sel_hi:[0,1,1]
	v_pk_fma_f32 v[26:27], v[54:55], v[90:91], v[26:27] op_sel_hi:[0,1,1]
	v_pk_fma_f32 v[64:65], v[54:55], v[92:93], v[70:71] op_sel_hi:[0,1,1]
	v_pk_fma_f32 v[24:25], v[54:55], v[94:95], v[24:25] op_sel_hi:[0,1,1]
	v_pk_fma_f32 v[66:67], v[54:55], v[96:97], v[72:73] op_sel_hi:[0,1,1]
	v_pk_fma_f32 v[22:23], v[54:55], v[98:99], v[22:23] op_sel_hi:[0,1,1]
	s_waitcnt vmcnt(15)
	v_cvt_pk_f32_fp8_e32 v[54:55], v49
	v_cvt_pk_f32_fp8_sdwa v[68:69], v49 src0_sel:WORD_1
	s_waitcnt vmcnt(14)
	v_cvt_pk_f32_fp8_e32 v[70:71], v132
	v_cvt_pk_f32_fp8_sdwa v[72:73], v132 src0_sel:WORD_1
	s_waitcnt vmcnt(13)
	v_cvt_pk_f32_fp8_e32 v[74:75], v133
	v_cvt_pk_f32_fp8_sdwa v[76:77], v133 src0_sel:WORD_1
	s_waitcnt vmcnt(12)
	v_cvt_pk_f32_fp8_e32 v[78:79], v134
	v_cvt_pk_f32_fp8_sdwa v[80:81], v134 src0_sel:WORD_1
	s_waitcnt vmcnt(11)
	v_cvt_pk_f32_fp8_e32 v[82:83], v135
	v_cvt_pk_f32_fp8_sdwa v[84:85], v135 src0_sel:WORD_1
	s_waitcnt vmcnt(10)
	v_cvt_pk_f32_fp8_e32 v[86:87], v136
	v_cvt_pk_f32_fp8_sdwa v[88:89], v136 src0_sel:WORD_1
	s_waitcnt vmcnt(9)
	v_cvt_pk_f32_fp8_e32 v[90:91], v137
	v_cvt_pk_f32_fp8_sdwa v[92:93], v137 src0_sel:WORD_1
	s_waitcnt vmcnt(8)
	v_cvt_pk_f32_fp8_e32 v[94:95], v138
	v_cvt_pk_f32_fp8_sdwa v[96:97], v138 src0_sel:WORD_1
	s_waitcnt vmcnt(7)
	v_cvt_pk_f32_fp8_e32 v[98:99], v139
	v_cvt_pk_f32_fp8_sdwa v[132:133], v139 src0_sel:WORD_1
	v_pk_fma_f32 v[46:47], v[50:51], v[100:101], v[46:47] op_sel_hi:[0,1,1]
	v_pk_fma_f32 v[36:37], v[50:51], v[102:103], v[36:37] op_sel_hi:[0,1,1]
	s_waitcnt vmcnt(6)
	v_cvt_pk_f32_fp8_e32 v[100:101], v140
	v_cvt_pk_f32_fp8_sdwa v[102:103], v140 src0_sel:WORD_1
	v_pk_fma_f32 v[52:53], v[50:51], v[104:105], v[52:53] op_sel_hi:[0,1,1]
	v_pk_fma_f32 v[34:35], v[50:51], v[106:107], v[34:35] op_sel_hi:[0,1,1]
	s_waitcnt vmcnt(5)
	v_cvt_pk_f32_fp8_e32 v[104:105], v141
	v_cvt_pk_f32_fp8_sdwa v[106:107], v141 src0_sel:WORD_1
	v_pk_fma_f32 v[56:57], v[50:51], v[108:109], v[56:57] op_sel_hi:[0,1,1]
	s_waitcnt vmcnt(4)
	v_cvt_pk_f32_fp8_e32 v[108:109], v142
	v_pk_fma_f32 v[58:59], v[50:51], v[112:113], v[58:59] op_sel_hi:[0,1,1]
	s_waitcnt vmcnt(3)
	v_cvt_pk_f32_fp8_e32 v[112:113], v143
	v_pk_fma_f32 v[60:61], v[50:51], v[116:117], v[60:61] op_sel_hi:[0,1,1]
	s_waitcnt vmcnt(2)
	v_cvt_pk_f32_fp8_e32 v[116:117], v144
	v_pk_fma_f32 v[62:63], v[50:51], v[120:121], v[62:63] op_sel_hi:[0,1,1]
	s_waitcnt vmcnt(1)
	v_cvt_pk_f32_fp8_e32 v[120:121], v145
	v_pk_fma_f32 v[64:65], v[50:51], v[124:125], v[64:65] op_sel_hi:[0,1,1]
	s_waitcnt vmcnt(0)
; __device__ __forceinline__ void p11_combine(const P& p, int gw, int NGW, int lane, float oscale) {
;     ...
;             for (int j = 0; j < 8; ++j) { const int w = (int)yr[64 * j]; const f32x2 lo = __builtin_amdgcn_cvt_pk_f32_fp8(w, false), hi = __builtin_amdgcn_cvt_pk_f32_fp8(w, true);
;                 a[j].x += g * lo.x; a[j].y += g * lo.y; a[j].z += g * hi.x; a[j].w += g * hi.y; } }
;         float ss = 0.f;
; #pragma unroll
;         for (int j = 0; j < 8; ++j) ss += (a[j].x * a[j].x + a[j].y * a[j].y) + (a[j].z * a[j].z + a[j].w * a[j].w);
;         ss = wave_sum(ss); const float r = rsqrtf(ss * (1.0f / DM) + EPS) * oscale;
	v_cvt_pk_f32_fp8_e32 v[124:125], v146
	v_pk_fma_f32 v[32:33], v[50:51], v[110:111], v[32:33] op_sel_hi:[0,1,1]
	v_cvt_pk_f32_fp8_sdwa v[110:111], v142 src0_sel:WORD_1
	v_pk_fma_f32 v[30:31], v[50:51], v[114:115], v[30:31] op_sel_hi:[0,1,1]
	v_cvt_pk_f32_fp8_sdwa v[114:115], v143 src0_sel:WORD_1
	v_pk_fma_f32 v[28:29], v[50:51], v[118:119], v[28:29] op_sel_hi:[0,1,1]
	v_cvt_pk_f32_fp8_sdwa v[118:119], v144 src0_sel:WORD_1
	v_pk_fma_f32 v[26:27], v[50:51], v[122:123], v[26:27] op_sel_hi:[0,1,1]
	v_cvt_pk_f32_fp8_sdwa v[122:123], v145 src0_sel:WORD_1
	v_pk_fma_f32 v[24:25], v[50:51], v[126:127], v[24:25] op_sel_hi:[0,1,1]
	v_cvt_pk_f32_fp8_sdwa v[126:127], v146 src0_sel:WORD_1
	v_pk_fma_f32 v[66:67], v[50:51], v[128:129], v[66:67] op_sel_hi:[0,1,1]
	v_pk_fma_f32 v[22:23], v[50:51], v[130:131], v[22:23] op_sel_hi:[0,1,1]
	v_pk_fma_f32 v[46:47], v[50:51], v[54:55], v[46:47] op_sel:[1,0,0]
	v_pk_fma_f32 v[36:37], v[50:51], v[68:69], v[36:37] op_sel:[1,0,0]
	v_pk_fma_f32 v[52:53], v[50:51], v[70:71], v[52:53] op_sel:[1,0,0]
	v_pk_fma_f32 v[34:35], v[50:51], v[72:73], v[34:35] op_sel:[1,0,0]
	v_pk_fma_f32 v[54:55], v[50:51], v[74:75], v[56:57] op_sel:[1,0,0]
	v_pk_fma_f32 v[32:33], v[50:51], v[76:77], v[32:33] op_sel:[1,0,0]
	v_pk_fma_f32 v[56:57], v[50:51], v[78:79], v[58:59] op_sel:[1,0,0]
	v_pk_fma_f32 v[30:31], v[50:51], v[80:81], v[30:31] op_sel:[1,0,0]
	v_pk_fma_f32 v[58:59], v[50:51], v[82:83], v[60:61] op_sel:[1,0,0]
	v_pk_fma_f32 v[28:29], v[50:51], v[84:85], v[28:29] op_sel:[1,0,0]
	v_pk_fma_f32 v[60:61], v[50:51], v[86:87], v[62:63] op_sel:[1,0,0]
	v_pk_fma_f32 v[26:27], v[50:51], v[88:89], v[26:27] op_sel:[1,0,0]
	v_pk_fma_f32 v[62:63], v[50:51], v[90:91], v[64:65] op_sel:[1,0,0]
	v_pk_fma_f32 v[24:25], v[50:51], v[92:93], v[24:25] op_sel:[1,0,0]
	v_pk_fma_f32 v[64:65], v[50:51], v[94:95], v[66:67] op_sel:[1,0,0]
	v_pk_fma_f32 v[22:23], v[50:51], v[96:97], v[22:23] op_sel:[1,0,0]
	v_pk_fma_f32 v[46:47], v[48:49], v[98:99], v[46:47] op_sel_hi:[0,1,1]
	v_pk_fma_f32 v[36:37], v[48:49], v[132:133], v[36:37] op_sel_hi:[0,1,1]
	v_pk_fma_f32 v[50:51], v[48:49], v[100:101], v[52:53] op_sel_hi:[0,1,1]
	v_pk_fma_f32 v[34:35], v[48:49], v[102:103], v[34:35] op_sel_hi:[0,1,1]
	v_pk_fma_f32 v[52:53], v[48:49], v[104:105], v[54:55] op_sel_hi:[0,1,1]
	v_pk_fma_f32 v[32:33], v[48:49], v[106:107], v[32:33] op_sel_hi:[0,1,1]
	v_pk_fma_f32 v[54:55], v[48:49], v[108:109], v[56:57] op_sel_hi:[0,1,1]
	v_pk_fma_f32 v[56:57], v[48:49], v[112:113], v[58:59] op_sel_hi:[0,1,1]
	v_pk_fma_f32 v[58:59], v[48:49], v[116:117], v[60:61] op_sel_hi:[0,1,1]
	v_pk_fma_f32 v[60:61], v[48:49], v[120:121], v[62:63] op_sel_hi:[0,1,1]
	v_pk_fma_f32 v[62:63], v[48:49], v[124:125], v[64:65] op_sel_hi:[0,1,1]
	v_mov_b32_e32 v64, v47
	v_mov_b32_e32 v65, v51
	v_mov_b32_e32 v68, v37
	v_mov_b32_e32 v69, v35
	v_pk_fma_f32 v[30:31], v[48:49], v[110:111], v[30:31] op_sel_hi:[0,1,1]
	v_pk_fma_f32 v[28:29], v[48:49], v[114:115], v[28:29] op_sel_hi:[0,1,1]
	v_pk_fma_f32 v[26:27], v[48:49], v[118:119], v[26:27] op_sel_hi:[0,1,1]
	v_pk_fma_f32 v[24:25], v[48:49], v[122:123], v[24:25] op_sel_hi:[0,1,1]
	v_pk_fma_f32 v[22:23], v[48:49], v[126:127], v[22:23] op_sel_hi:[0,1,1]
	v_mov_b32_e32 v48, v46
	v_mov_b32_e32 v49, v50
	v_mov_b32_e32 v66, v36
	v_mov_b32_e32 v67, v34
	v_mov_b32_e32 v72, v53
	v_mov_b32_e32 v73, v33
	v_pk_mul_f32 v[64:65], v[64:65], v[64:65]
	v_pk_mul_f32 v[68:69], v[68:69], v[68:69]
	v_mov_b32_e32 v70, v52
	v_mov_b32_e32 v71, v32
	v_pk_mul_f32 v[72:73], v[72:73], v[72:73]
	v_pk_fma_f32 v[48:49], v[48:49], v[48:49], v[64:65]
	v_pk_fma_f32 v[64:65], v[66:67], v[66:67], v[68:69]
	v_mul_f32_e32 v74, v55, v55
	v_mul_f32_e32 v76, v31, v31
	v_pk_fma_f32 v[66:67], v[70:71], v[70:71], v[72:73]
	v_pk_add_f32 v[48:49], v[48:49], v[64:65]
	v_pk_mul_f32 v[78:79], v[56:57], v[56:57]
	v_pk_mul_f32 v[80:81], v[28:29], v[28:29]
	v_pk_fma_f32 v[74:75], v[54:55], v[54:55], v[74:75] op_sel_hi:[1,1,0]
	v_pk_fma_f32 v[76:77], v[30:31], v[30:31], v[76:77] op_sel_hi:[1,1,0]
	v_pk_add_f32 v[64:65], v[66:67], v[66:67] op_sel:[0,1] op_sel_hi:[1,0]
	v_pk_add_f32 v[48:49], v[48:49], v[48:49] op_sel:[0,1] op_sel_hi:[1,0]
	v_mov_b32_e32 v84, v59
	v_mov_b32_e32 v85, v27
	v_mov_b32_e32 v75, v80
	v_mov_b32_e32 v77, v81
	v_mov_b32_e32 v65, v79
	v_mov_b32_e32 v49, v78
	v_mov_b32_e32 v82, v58
	v_mov_b32_e32 v83, v26
	v_pk_mul_f32 v[84:85], v[84:85], v[84:85]
	v_pk_add_f32 v[66:67], v[74:75], v[76:77]
	v_pk_add_f32 v[48:49], v[48:49], v[64:65]
	v_mul_f32_e32 v86, v61, v61
	v_mul_f32_e32 v88, v25, v25
	v_pk_fma_f32 v[68:69], v[82:83], v[82:83], v[84:85]
	v_pk_add_f32 v[48:49], v[48:49], v[66:67]
	v_pk_mul_f32 v[90:91], v[62:63], v[62:63]
	v_pk_mul_f32 v[92:93], v[22:23], v[22:23]
	v_pk_fma_f32 v[86:87], v[60:61], v[60:61], v[86:87] op_sel_hi:[1,1,0]
	v_pk_fma_f32 v[88:89], v[24:25], v[24:25], v[88:89] op_sel_hi:[1,1,0]
	v_pk_add_f32 v[68:69], v[68:69], v[68:69] op_sel:[0,1] op_sel_hi:[1,0]
	v_pk_add_f32 v[48:49], v[48:49], v[48:49] op_sel:[0,1] op_sel_hi:[1,0]
	v_mov_b32_e32 v87, v92
	v_mov_b32_e32 v89, v93
	v_mov_b32_e32 v69, v91
	v_mov_b32_e32 v49, v90
	v_pk_add_f32 v[70:71], v[86:87], v[88:89]
	v_pk_add_f32 v[48:49], v[48:49], v[68:69]
	s_nop 0
	v_pk_add_f32 v[48:49], v[48:49], v[70:71]
	s_nop 0
	v_add_f32_e32 v48, v48, v49
	ds_bpermute_b32 v49, v40, v48
	s_waitcnt lgkmcnt(0)
; #define GAS __attribute__((address_space(1)))
; __device__ __forceinline__ void p11_combine(const P& p, int gw, int NGW, int lane, float oscale) {
;     ...
;         ss = wave_sum(ss); const float r = rsqrtf(ss * (1.0f / DM) + EPS) * oscale;
;         const GAS f32x4* gf = (const GAS f32x4*)p.g_fin + lane;
; #pragma unroll
;         for (int j = 0; j < 8; ++j) { const f32x4 g = gf[64 * j]; xr[64 * j] = a[j] * r * g; }
	v_add_f32_e32 v48, v48, v49
	ds_bpermute_b32 v49, v41, v48
	s_waitcnt lgkmcnt(0)
	v_add_f32_e32 v48, v48, v49
	ds_bpermute_b32 v49, v42, v48
	s_waitcnt lgkmcnt(0)
	v_add_f32_e32 v48, v48, v49
	ds_bpermute_b32 v49, v43, v48
	s_waitcnt lgkmcnt(0)
	v_add_f32_e32 v48, v48, v49
	ds_bpermute_b32 v49, v44, v48
	s_waitcnt lgkmcnt(0)
	v_add_f32_e32 v48, v48, v49
	ds_bpermute_b32 v49, v45, v48
	s_waitcnt lgkmcnt(0)
	v_add_f32_e32 v48, v48, v49
	v_fmamk_f32 v48, v48, 0x3a000000, v4
	v_mul_f32_e32 v49, 0x4b800000, v48
	v_cmp_gt_f32_e32 vcc, s13, v48
	s_nop 1
	v_cndmask_b32_e32 v48, v48, v49, vcc
	v_rsq_f32_e32 v48, v48
	s_nop 0
	v_mul_f32_e32 v49, 0x45800000, v48
	v_cndmask_b32_e32 v48, v48, v49, vcc
	v_pk_mul_f32 v[46:47], v[46:47], v[48:49] op_sel_hi:[1,0]
	v_pk_mul_f32 v[36:37], v[36:37], v[48:49] op_sel_hi:[1,0]
	v_pk_mul_f32 v[0:1], v[0:1], v[46:47]
	v_pk_mul_f32 v[2:3], v[2:3], v[36:37]
	global_store_dwordx4 v[18:19], v[0:3], off offset:-4096
	v_pk_mul_f32 v[34:35], v[34:35], v[48:49] op_sel_hi:[1,0]
	v_pk_mul_f32 v[36:37], v[50:51], v[48:49] op_sel_hi:[1,0]
	v_pk_mul_f32 v[32:33], v[32:33], v[48:49] op_sel_hi:[1,0]
	v_pk_mul_f32 v[30:31], v[30:31], v[48:49] op_sel_hi:[1,0]
	v_pk_mul_f32 v[28:29], v[28:29], v[48:49] op_sel_hi:[1,0]
	v_pk_mul_f32 v[26:27], v[26:27], v[48:49] op_sel_hi:[1,0]
	v_pk_mul_f32 v[24:25], v[24:25], v[48:49] op_sel_hi:[1,0]
	v_pk_mul_f32 v[22:23], v[22:23], v[48:49] op_sel_hi:[1,0]
	v_pk_mul_f32 v[192:193], v[164:165], v[36:37]
	v_pk_mul_f32 v[194:195], v[166:167], v[34:35]
	global_store_dwordx4 v[18:19], v[192:195], off offset:-3072
	v_pk_mul_f32 v[34:35], v[52:53], v[48:49] op_sel_hi:[1,0]
	v_pk_mul_f32 v[2:3], v[170:171], v[32:33]
	v_pk_mul_f32 v[0:1], v[168:169], v[34:35]
	global_store_dwordx4 v[18:19], v[0:3], off offset:-2048
	v_pk_mul_f32 v[32:33], v[54:55], v[48:49] op_sel_hi:[1,0]
	v_pk_mul_f32 v[194:195], v[174:175], v[30:31]
	v_pk_mul_f32 v[192:193], v[172:173], v[32:33]
	global_store_dwordx4 v[18:19], v[192:195], off offset:-1024
	v_pk_mul_f32 v[30:31], v[56:57], v[48:49] op_sel_hi:[1,0]
	v_pk_mul_f32 v[2:3], v[178:179], v[28:29]
	v_pk_mul_f32 v[0:1], v[176:177], v[30:31]
	global_store_dwordx4 v[18:19], v[0:3], off
	v_pk_mul_f32 v[28:29], v[58:59], v[48:49] op_sel_hi:[1,0]
	v_pk_mul_f32 v[194:195], v[182:183], v[26:27]
	v_pk_mul_f32 v[192:193], v[180:181], v[28:29]
	global_store_dwordx4 v[18:19], v[192:195], off offset:1024
	v_pk_mul_f32 v[26:27], v[60:61], v[48:49] op_sel_hi:[1,0]
	v_pk_mul_f32 v[2:3], v[186:187], v[24:25]
	v_pk_mul_f32 v[0:1], v[184:185], v[26:27]
	global_store_dwordx4 v[18:19], v[0:3], off offset:2048
	v_pk_mul_f32 v[24:25], v[62:63], v[48:49] op_sel_hi:[1,0]
	v_pk_mul_f32 v[194:195], v[190:191], v[22:23]
	v_pk_mul_f32 v[192:193], v[188:189], v[24:25]
	global_store_dwordx4 v[18:19], v[192:195], off offset:3072
	v_lshl_add_u64 v[18:19], v[18:19], 0, s[2:3]
	s_cbranch_scc1 .LBB5_1742
